# speedup vs baseline: 1.1405x; 1.0058x over previous
_Z6k_prepPKfS0_S0_S0_S0_S0_S0_S0_S0_S0_S0_S0_S0_PDv8_DF16_S2_S2_PfS0_:
	s_cmpk_lt_u32 s2, 0x468
	s_cbranch_scc0 .Lmy_norot
	s_add_i32 s4, s2, 0x460
	s_add_i32 s5, s2, -8
	s_cmp_lt_u32 s2, 8
	s_cselect_b32 s2, s4, s5
.Lmy_norot:
	s_cmpk_lt_u32 s2, 0x468
	s_mov_b64 s[4:5], -1
	s_cbranch_scc1 .LBB0_3
	s_andn2_b64 vcc, exec, s[4:5]
	s_cbranch_vccz .LBB0_46
